# stack6: stack5 plus dense-down epilogue residual rows prefetched with counted waits, final combine loop store drain removed
# baseline (speedup 1.0000x reference)
; __device__ __forceinline__ float wave_sum(float v) {
; #pragma unroll
;     for (int o = 1; o < 64; o <<= 1) v += __shfl_xor(v, o);
;     return v;
; __device__ __forceinline__ void phase_final(const bf16_t* XA, const bf16_t* Y, const int* tok_info, const float* g, float* out, int wid, int lane) {
;     const int gw = blockIdx.x * 8 + wid, NGW = gridDim.x * 8;
;     f32x4 gg[8];
; #pragma unroll
;     for (int j = 0; j < 8; ++j) gg[j] = *(const f32x4*)(g + 4 * lane + 256 * j);
;     if (gw >= T) return;
;     int c1 = tok_info[(size_t)gw * 8 + 6], c2 = tok_info[(size_t)gw * 8 + 7];
;     u32x2 xr[8], ya[8], yb[8];
; #pragma unroll
;     for (int j = 0; j < 8; ++j) { const int o = 4 * lane + 256 * j; xr[j] = *(const u32x2*)(XA + (size_t)gw * D + o); ya[j] = *(const u32x2*)(Y + (size_t)c1 * D + o); yb[j] = *(const u32x2*)(Y + (size_t)c2 * D + o); }
;     int e1 = c1, e2 = c2; { const int t2 = gw + NGW; if (t2 < T) { e1 = tok_info[(size_t)t2 * 8 + 6]; e2 = tok_info[(size_t)t2 * 8 + 7]; } }
;     for (int t = gw; t < T; t += NGW) {
;         const int tn = t + NGW; const bool okn = tn < T; const int tc = okn ? tn : t;
;         u32x2 nx[8], na[8], nb[8];
; #pragma unroll
;         for (int j = 0; j < 8; ++j) { const int o = 4 * lane + 256 * j; nx[j] = *(const u32x2*)(XA + (size_t)tc * D + o); na[j] = *(const u32x2*)(Y + (size_t)e1 * D + o); nb[j] = *(const u32x2*)(Y + (size_t)e2 * D + o); }
.LBB0_2982:
	v_cmp_lt_i32_e32 vcc, v202, v195
	v_lshl_add_u64 v[38:39], s[6:7], 0, v[2:3]
	s_nop 0
	v_cndmask_b32_e32 v36, v194, v202, vcc
	v_cmp_lt_i32_e32 vcc, v192, v195
	v_lshlrev_b32_e32 v140, 2, v36
	s_nop 0
	v_cndmask_b32_e32 v36, v194, v192, vcc
	v_cmp_lt_i32_e32 vcc, v200, v195
	v_lshlrev_b32_e32 v141, 2, v36
	s_nop 0
	v_cndmask_b32_e32 v36, v194, v200, vcc
	v_lshlrev_b32_e32 v142, 2, v36
	v_xor_b32_e32 v36, 8, v194
	v_cmp_lt_i32_e32 vcc, v36, v195
	s_nop 1
	v_cndmask_b32_e32 v36, v194, v36, vcc
	v_lshlrev_b32_e32 v143, 2, v36
	v_xor_b32_e32 v36, 16, v194
	v_cmp_lt_i32_e32 vcc, v36, v195
	s_nop 1
	v_cndmask_b32_e32 v36, v194, v36, vcc
	v_lshlrev_b32_e32 v144, 2, v36
	v_xor_b32_e32 v36, 32, v194
	v_cmp_lt_i32_e32 vcc, v36, v195
	s_nop 1
	v_cndmask_b32_e32 v36, v194, v36, vcc
	v_lshlrev_b32_e32 v145, 2, v36
	v_lshl_add_u64 v[36:37], s[2:3], 0, v[2:3]
	s_lshl_b64 s[2:3], s[4:5], 13
	v_readlane_b32 s5, v254, 24
	v_and_b32_e32 v2, 63, v40
	s_add_u32 s2, s5, s2
	v_readlane_b32 s5, v254, 25
	v_lshlrev_b32_e32 v2, 4, v2
	s_addc_u32 s3, s5, s3
	v_lshl_add_u64 v[40:41], s[2:3], 0, v[2:3]
	s_waitcnt vmcnt(0)
	s_branch .LBB0_2984

; __device__ __forceinline__ void phase_final(const bf16_t* XA, const bf16_t* Y, const int* tok_info, const float* g, float* out, int wid, int lane) {
;     ...
;     for (int t = gw; t < T; t += NGW) {
;         const int tn = t + NGW; const bool okn = tn < T; const int tc = okn ? tn : t;
;         u32x2 nx[8], na[8], nb[8];
; #pragma unroll
;         for (int j = 0; j < 8; ++j) { const int o = 4 * lane + 256 * j; nx[j] = *(const u32x2*)(XA + (size_t)tc * D + o); na[j] = *(const u32x2*)(Y + (size_t)e1 * D + o); nb[j] = *(const u32x2*)(Y + (size_t)e2 * D + o); }
;         int f1 = e1, f2 = e2; { const int t3 = t + 2 * NGW; if (t3 < T) { f1 = tok_info[(size_t)t3 * 8 + 6]; f2 = tok_info[(size_t)t3 * 8 + 7]; } }
.LBB0_2984:
	v_readlane_b32 s2, v254, 33
	s_mov_b32 s5, s4
	s_add_i32 s4, s2, s4
	s_cmpk_lt_i32 s4, 0x4000
	v_readlane_b32 s3, v254, 34
	s_cselect_b32 s2, s4, s5
	s_ashr_i32 s3, s2, 31
	s_waitcnt vmcnt(8)
	v_ashrrev_i32_e32 v43, 31, v0
	v_mov_b32_e32 v42, v0
	v_ashrrev_i32_e32 v45, 31, v1
	v_mov_b32_e32 v44, v1
	s_lshl_b64 s[2:3], s[2:3], 12
	v_lshlrev_b64 v[42:43], 12, v[42:43]
	v_lshlrev_b64 v[44:45], 12, v[44:45]
	v_lshl_add_u64 v[68:69], v[36:37], 0, s[2:3]
	v_lshl_add_u64 v[86:87], v[38:39], 0, v[42:43]
	v_lshl_add_u64 v[98:99], v[38:39], 0, v[44:45]
	global_load_dwordx2 v[42:43], v[68:69], off
	global_load_dwordx2 v[44:45], v[68:69], off offset:512
	global_load_dwordx2 v[46:47], v[68:69], off offset:1024
	global_load_dwordx2 v[48:49], v[68:69], off offset:1536
	global_load_dwordx2 v[56:57], v[86:87], off
	global_load_dwordx2 v[58:59], v[86:87], off offset:512
	global_load_dwordx2 v[60:61], v[86:87], off offset:1024
	global_load_dwordx2 v[62:63], v[86:87], off offset:1536
	global_load_dwordx2 v[70:71], v[98:99], off
	global_load_dwordx2 v[72:73], v[98:99], off offset:512
	global_load_dwordx2 v[74:75], v[98:99], off offset:1024
	global_load_dwordx2 v[76:77], v[98:99], off offset:1536
	global_load_dwordx2 v[50:51], v[68:69], off offset:2048
	global_load_dwordx2 v[54:55], v[68:69], off offset:2560
	global_load_dwordx2 v[64:65], v[68:69], off offset:3072
	s_nop 0
	global_load_dwordx2 v[68:69], v[68:69], off offset:3584
	s_nop 0
	global_load_dwordx2 v[80:81], v[86:87], off offset:2048
	global_load_dwordx2 v[82:83], v[86:87], off offset:2560
	global_load_dwordx2 v[84:85], v[86:87], off offset:3072
	s_nop 0
	global_load_dwordx2 v[86:87], v[86:87], off offset:3584
	s_nop 0
	global_load_dwordx2 v[88:89], v[98:99], off offset:2048
	global_load_dwordx2 v[90:91], v[98:99], off offset:2560
	global_load_dwordx2 v[94:95], v[98:99], off offset:3072
	s_nop 0
	global_load_dwordx2 v[98:99], v[98:99], off offset:3584
	v_readlane_b32 s2, v253, 40
	s_add_i32 s2, s2, s5
	s_cmpk_gt_i32 s2, 0x3fff
	s_cbranch_scc1 .LBB0_2983
	s_ashr_i32 s3, s2, 31
	s_lshl_b64 s[2:3], s[2:3], 5
	s_add_u32 s2, s0, s2
	s_addc_u32 s3, s10, s3
	global_load_dwordx2 v[0:1], v3, s[2:3] offset:24
	s_branch .LBB0_2983

; __device__ __forceinline__ float bflo(unsigned x) { return __uint_as_float(x << 16); }
; __device__ __forceinline__ float bfhi(unsigned x) { return __uint_as_float(x & 0xffff0000u); }
;     __device__ __forceinline__ void operator()(const f32x4 (&acc)[2][2][4][2], const Unit& u, int wr, int wc, int fr, int fq) const {
;     ...
; #pragma unroll
;         for (int ai = 0; ai < 2; ++ai)
; #pragma unroll
;           for (int mh = 0; mh < 2; ++mh) {
;             f32x4 r[2][2][2];
; #pragma unroll
;             for (int mm = 0; mm < 2; ++mm) { const int m = 2 * mh + mm; const size_t off = (size_t)(row0 + ai * HALF + m * 16) * ldc + col0;
; #pragma unroll
;                 for (int bj = 0; bj < 2; ++bj) {
;                     if constexpr (RF32) { const float* p = (const float*)res + off + bj * HALF; r[mm][bj][0] = *(const f32x4*)p; r[mm][bj][1] = *(const f32x4*)(p + 4); }
;                     else { const u32x4 w = *(const u32x4*)((const bf16_t*)res + off + bj * HALF); r[mm][bj][0] = (f32x4){bflo(w.x), bfhi(w.x), bflo(w.y), bfhi(w.y)}; r[mm][bj][1] = (f32x4){bflo(w.z), bfhi(w.z), bflo(w.w), bfhi(w.w)}; } } }
;             asm volatile("" ::: "memory");
; #pragma unroll
;             for (int mm = 0; mm < 2; ++mm) { const int m = 2 * mh + mm; const size_t off = (size_t)(row0 + ai * HALF + m * 16) * ldc + col0; float sq = 0.f;
; #pragma unroll
;                 for (int bj = 0; bj < 2; ++bj) { const f32x4 v0 = r[mm][bj][0] + acc[ai][bj][m][0], v1 = r[mm][bj][1] + acc[ai][bj][m][1];
;                     u32x4 w; w.x = cvtpk(v0[0], v0[1]); w.y = cvtpk(v0[2], v0[3]); w.z = cvtpk(v1[0], v1[1]); w.w = cvtpk(v1[2], v1[3]);
;                     *(u32x4*)(out + off + bj * HALF) = w;
;                     const float a0 = bflo(w.x), a1 = bfhi(w.x), a2 = bflo(w.y), a3 = bfhi(w.y), a4 = bflo(w.z), a5 = bfhi(w.z), a6 = bflo(w.w), a7 = bfhi(w.w);
;                     if (out8) { u32x2 w8; w8.x = pk4_fp8(a0, a1, a2, a3); w8.y = pk4_fp8(a4, a5, a6, a7); *(u32x2*)(out8 + off + bj * HALF) = w8; }
;                     sq += ((a0 * a0 + a1 * a1) + (a2 * a2 + a3 * a3)) + ((a4 * a4 + a5 * a5) + (a6 * a6 + a7 * a7)); }
;                 if (ss) { sq += __shfl_xor(sq, 16); sq += __shfl_xor(sq, 32); if (fq == 0) ss[(size_t)(row0 + ai * HALF + m * 16) * 32 + 4 * u.pn + wc] = sq; } }
.LBB0_3134:
	v_lshl_add_u32 v144, s54, 8, v141
	v_lshl_or_b32 v142, s0, 8, v150
	v_ashrrev_i32_e32 v143, 31, v142
	v_ashrrev_i32_e32 v145, 31, v144
	v_lshl_add_u64 v[146:147], v[142:143], 1, s[8:9]
	v_lshlrev_b64 v[132:133], 12, v[144:145]
	v_lshl_add_u64 v[132:133], v[146:147], 0, v[132:133]
	global_load_dwordx4 v[154:157], v[132:133], off
	global_load_dwordx4 v[158:161], v[132:133], off offset:256
	v_or_b32_e32 v148, 16, v144
	v_ashrrev_i32_e32 v149, 31, v148
	v_lshlrev_b64 v[132:133], 11, v[144:145]
	v_lshlrev_b64 v[134:135], 12, v[148:149]
	v_readlane_b32 s56, v250, 34
	v_lshl_add_u64 v[132:133], v[132:133], 0, v[142:143]
	v_lshl_add_u64 v[134:135], v[146:147], 0, v[134:135]
	v_readlane_b32 s70, v250, 48
	v_readlane_b32 s71, v250, 49
	v_lshl_add_u64 v[168:169], s[12:13], 0, v[132:133]
	v_mov_b32_e32 v162, v3
	v_lshl_add_u64 v[166:167], v[132:133], 1, s[70:71]
	global_load_dwordx4 v[136:139], v[134:135], off
	s_nop 0
	global_load_dwordx4 v[132:135], v[134:135], off offset:256
	v_lshlrev_b64 v[180:181], 12, v[144:145]
	v_lshl_add_u64 v[180:181], v[146:147], 0, v[180:181]
	s_mov_b64 s[72:73], 0x20000
	v_lshl_add_u64 v[182:183], s[72:73], 0, v[180:181]
	global_load_dwordx4 v[206:209], v[182:183], off
	global_load_dwordx4 v[210:213], v[182:183], off offset:256
	s_mov_b64 s[72:73], 0x30000
	v_lshl_add_u64 v[182:183], s[72:73], 0, v[180:181]
	global_load_dwordx4 v[214:217], v[182:183], off
	global_load_dwordx4 v[218:221], v[182:183], off offset:256
	s_mov_b64 s[72:73], 0x80000
	v_lshl_add_u64 v[182:183], s[72:73], 0, v[180:181]
	global_load_dwordx4 v[222:225], v[182:183], off
	global_load_dwordx4 v[226:229], v[182:183], off offset:256
	s_mov_b64 s[72:73], 0x90000
	v_lshl_add_u64 v[182:183], s[72:73], 0, v[180:181]
	global_load_dwordx4 v[230:233], v[182:183], off
	global_load_dwordx4 v[234:237], v[182:183], off offset:256
	v_mov_b32_e32 v163, v3
	v_mov_b32_e32 v164, v3
	v_mov_b32_e32 v165, v3
	s_lshl_b32 s20, s0, 2
	s_ashr_i32 s21, s20, 31
	v_readlane_b32 s57, v250, 35
	v_readlane_b32 s58, v250, 36
	v_readlane_b32 s59, v250, 37
	v_readlane_b32 s60, v250, 38
	v_readlane_b32 s61, v250, 39
	v_readlane_b32 s62, v250, 40
	v_readlane_b32 s63, v250, 41
	v_readlane_b32 s64, v250, 42
	v_readlane_b32 s65, v250, 43
	v_readlane_b32 s66, v250, 44
	v_readlane_b32 s67, v250, 45
	v_readlane_b32 s68, v250, 46
	v_readlane_b32 s69, v250, 47
	s_waitcnt vmcnt(11)
	v_lshlrev_b32_e32 v170, 16, v154
	v_and_b32_e32 v171, 0xffff0000, v154
	v_lshlrev_b32_e32 v154, 16, v155
	v_and_b32_e32 v155, 0xffff0000, v155
	v_lshlrev_b32_e32 v172, 16, v156
	v_and_b32_e32 v173, 0xffff0000, v156
	v_lshlrev_b32_e32 v156, 16, v157
	v_and_b32_e32 v157, 0xffff0000, v157
	s_waitcnt vmcnt(10)
	v_lshlrev_b32_e32 v176, 16, v160
	v_and_b32_e32 v177, 0xffff0000, v160
	v_lshlrev_b32_e32 v160, 16, v161
	v_and_b32_e32 v161, 0xffff0000, v161
	v_pk_add_f32 v[130:131], v[130:131], v[154:155]
	v_pk_add_f32 v[128:129], v[128:129], v[170:171]
	v_pk_add_f32 v[126:127], v[126:127], v[156:157]
	v_pk_add_f32 v[124:125], v[124:125], v[172:173]
	v_pk_add_f32 v[154:155], v[118:119], v[160:161]
	v_pk_add_f32 v[156:157], v[116:117], v[176:177]
	v_cvt_pk_bf16_f32 v116, v128, v129
	v_cvt_pk_bf16_f32 v117, v130, v131
	v_cvt_pk_bf16_f32 v118, v124, v125
	v_cvt_pk_bf16_f32 v119, v126, v127
	global_store_dwordx4 v[166:167], v[116:119], off
	v_lshlrev_b32_e32 v124, 16, v116
	v_lshlrev_b32_e32 v126, 16, v118
	v_and_b32_e32 v116, 0xffff0000, v116
	v_and_b32_e32 v118, 0xffff0000, v118
	v_cvt_pk_fp8_f32 v162, v124, v116
	v_cvt_pk_fp8_f32 v163, v126, v118
	v_lshlrev_b32_e32 v125, 16, v117
	v_and_b32_e32 v117, 0xffff0000, v117
	v_lshlrev_b32_e32 v127, 16, v119
	v_and_b32_e32 v119, 0xffff0000, v119
	v_cvt_pk_fp8_f32 v162, v125, v117 op_sel:[0,0,1]
	v_cvt_pk_fp8_f32 v163, v127, v119 op_sel:[0,0,1]
	v_mul_f32_e32 v116, v116, v116
	v_mul_f32_e32 v128, v117, v117
	v_mul_f32_e32 v118, v118, v118
	v_mul_f32_e32 v129, v119, v119
	v_lshlrev_b32_e32 v174, 16, v158
	v_and_b32_e32 v175, 0xffff0000, v158
	v_lshlrev_b32_e32 v158, 16, v159
	v_and_b32_e32 v159, 0xffff0000, v159
	v_fmac_f32_e32 v116, v124, v124
	v_fmac_f32_e32 v128, v125, v125
	v_fmac_f32_e32 v118, v126, v126
	v_fmac_f32_e32 v129, v127, v127
	v_pk_add_f32 v[122:123], v[122:123], v[158:159]
	v_pk_add_f32 v[120:121], v[120:121], v[174:175]
	v_add_f32_e32 v116, v116, v128
	v_add_f32_e32 v117, v118, v129
	v_add_f32_e32 v116, v116, v117
	global_store_dwordx2 v[168:169], v[162:163], off
	v_cvt_pk_bf16_f32 v120, v120, v121
	v_cvt_pk_bf16_f32 v121, v122, v123
	v_cvt_pk_bf16_f32 v122, v156, v157
	v_cvt_pk_bf16_f32 v123, v154, v155
	s_nop 0
	v_lshlrev_b32_e32 v117, 16, v120
	v_and_b32_e32 v118, 0xffff0000, v120
	v_and_b32_e32 v124, 0xffff0000, v121
	v_lshlrev_b32_e32 v125, 16, v122
	v_and_b32_e32 v126, 0xffff0000, v122
	v_and_b32_e32 v128, 0xffff0000, v123
	v_lshlrev_b32_e32 v119, 16, v121
	v_lshlrev_b32_e32 v127, 16, v123
	v_cvt_pk_fp8_f32 v164, v117, v118
	v_cvt_pk_fp8_f32 v165, v125, v126
	v_mul_f32_e32 v118, v118, v118
	v_mul_f32_e32 v129, v124, v124
	v_mul_f32_e32 v126, v126, v126
	v_mul_f32_e32 v130, v128, v128
	v_fmac_f32_e32 v118, v117, v117
	v_fmac_f32_e32 v129, v119, v119
	v_fmac_f32_e32 v126, v125, v125
	v_fmac_f32_e32 v130, v127, v127
	v_add_f32_e32 v117, v118, v129
	v_add_f32_e32 v118, v126, v130
	v_add_f32_e32 v117, v117, v118
	v_add_f32_e32 v117, v116, v117
	v_xor_b32_e32 v116, 16, v194
	v_cmp_lt_i32_e32 vcc, v116, v195
	v_cvt_pk_fp8_f32 v164, v119, v124 op_sel:[0,0,1]
	v_cvt_pk_fp8_f32 v165, v127, v128 op_sel:[0,0,1]
	v_cndmask_b32_e32 v116, v194, v116, vcc
	v_lshlrev_b32_e32 v116, 2, v116
	ds_bpermute_b32 v118, v116, v117
	global_store_dwordx4 v[166:167], v[120:123], off offset:256
	global_store_dwordx2 v[168:169], v[164:165], off offset:128
	s_waitcnt lgkmcnt(0)
	v_add_f32_e32 v118, v117, v118
	v_xor_b32_e32 v117, 32, v194
	v_cmp_lt_i32_e32 vcc, v117, v195
	s_nop 1
	v_cndmask_b32_e32 v117, v194, v117, vcc
	v_lshlrev_b32_e32 v117, 2, v117
	ds_bpermute_b32 v119, v117, v118
	s_and_saveexec_b64 s[22:23], s[2:3]
	s_cbranch_execz .LBB0_3136
	v_lshlrev_b64 v[120:121], 7, v[144:145]
	v_lshl_add_u64 v[120:121], s[10:11], 0, v[120:121]
	v_lshl_add_u64 v[120:121], s[20:21], 2, v[120:121]
	s_lshl_b32 s0, s42, 2
	v_lshl_add_u64 v[120:121], v[120:121], 0, s[0:1]
	s_waitcnt lgkmcnt(0)
	v_add_f32_e32 v118, v118, v119
	global_store_dword v[120:121], v118, off
; __device__ __forceinline__ float bflo(unsigned x) { return __uint_as_float(x << 16); }
; __device__ __forceinline__ float bfhi(unsigned x) { return __uint_as_float(x & 0xffff0000u); }
; __device__ __forceinline__ unsigned cvtpk(float lo, float hi) { unsigned r; asm volatile("v_cvt_pk_bf16_f32 %0, %1, %2" : "=v"(r) : "v"(lo), "v"(hi)); return r; }
;     __device__ __forceinline__ void operator()(const f32x4 (&acc)[2][2][4][2], const Unit& u, int wr, int wc, int fr, int fq) const {
;     ...
;             for (int mm = 0; mm < 2; ++mm) { const int m = 2 * mh + mm; const size_t off = (size_t)(row0 + ai * HALF + m * 16) * ldc + col0;
; #pragma unroll
;                 for (int bj = 0; bj < 2; ++bj) {
;                     if constexpr (RF32) { const float* p = (const float*)res + off + bj * HALF; r[mm][bj][0] = *(const f32x4*)p; r[mm][bj][1] = *(const f32x4*)(p + 4); }
;                     else { const u32x4 w = *(const u32x4*)((const bf16_t*)res + off + bj * HALF); r[mm][bj][0] = (f32x4){bflo(w.x), bfhi(w.x), bflo(w.y), bfhi(w.y)}; r[mm][bj][1] = (f32x4){bflo(w.z), bfhi(w.z), bflo(w.w), bfhi(w.w)}; } } }
;             asm volatile("" ::: "memory");
; #pragma unroll
;             for (int mm = 0; mm < 2; ++mm) { const int m = 2 * mh + mm; const size_t off = (size_t)(row0 + ai * HALF + m * 16) * ldc + col0; float sq = 0.f;
; #pragma unroll
;                 for (int bj = 0; bj < 2; ++bj) { const f32x4 v0 = r[mm][bj][0] + acc[ai][bj][m][0], v1 = r[mm][bj][1] + acc[ai][bj][m][1];
;                     u32x4 w; w.x = cvtpk(v0[0], v0[1]); w.y = cvtpk(v0[2], v0[3]); w.z = cvtpk(v1[0], v1[1]); w.w = cvtpk(v1[2], v1[3]);
;                     *(u32x4*)(out + off + bj * HALF) = w;
;                     const float a0 = bflo(w.x), a1 = bfhi(w.x), a2 = bflo(w.y), a3 = bfhi(w.y), a4 = bflo(w.z), a5 = bfhi(w.z), a6 = bflo(w.w), a7 = bfhi(w.w);
;                     if (out8) { u32x2 w8; w8.x = pk4_fp8(a0, a1, a2, a3); w8.y = pk4_fp8(a4, a5, a6, a7); *(u32x2*)(out8 + off + bj * HALF) = w8; }
;                     sq += ((a0 * a0 + a1 * a1) + (a2 * a2 + a3 * a3)) + ((a4 * a4 + a5 * a5) + (a6 * a6 + a7 * a7)); }
;                 if (ss) { sq += __shfl_xor(sq, 16); sq += __shfl_xor(sq, 32); if (fq == 0) ss[(size_t)(row0 + ai * HALF + m * 16) * 32 + 4 * u.pn + wc] = sq; } }
.LBB0_3136:
	s_or_b64 exec, exec, s[22:23]
	s_waitcnt vmcnt(13)
	v_lshlrev_b32_e32 v120, 16, v136
	v_and_b32_e32 v121, 0xffff0000, v136
	v_lshlrev_b32_e32 v124, 16, v138
	v_and_b32_e32 v125, 0xffff0000, v138
	v_lshlrev_b32_e32 v126, 16, v139
	v_and_b32_e32 v127, 0xffff0000, v139
	v_lshlrev_b32_e32 v122, 16, v137
	v_and_b32_e32 v123, 0xffff0000, v137
	v_pk_add_f32 v[112:113], v[112:113], v[120:121]
	v_pk_add_f32 v[120:121], v[110:111], v[126:127]
	v_pk_add_f32 v[110:111], v[108:109], v[124:125]
	v_pk_add_f32 v[114:115], v[114:115], v[122:123]
	v_cvt_pk_bf16_f32 v108, v112, v113
	v_mov_b32_e32 v112, v3
	v_cvt_pk_bf16_f32 v109, v114, v115
	v_cvt_pk_bf16_f32 v110, v110, v111
	v_cvt_pk_bf16_f32 v111, v120, v121
	v_lshlrev_b32_e32 v120, 16, v108
	v_and_b32_e32 v121, 0xffff0000, v108
	v_lshlrev_b32_e32 v124, 16, v110
	v_and_b32_e32 v125, 0xffff0000, v110
	v_mov_b32_e32 v113, v3
	v_cvt_pk_fp8_f32 v112, v120, v121
	v_cvt_pk_fp8_f32 v113, v124, v125
	s_waitcnt lgkmcnt(0)
	v_lshlrev_b64 v[118:119], 11, v[148:149]
	v_lshlrev_b32_e32 v122, 16, v109
	v_and_b32_e32 v123, 0xffff0000, v109
	v_lshlrev_b32_e32 v126, 16, v111
	v_and_b32_e32 v127, 0xffff0000, v111
	v_readlane_b32 s56, v250, 34
	v_lshl_add_u64 v[118:119], v[118:119], 0, v[142:143]
	v_cvt_pk_fp8_f32 v112, v122, v123 op_sel:[0,0,1]
	v_cvt_pk_fp8_f32 v113, v126, v127 op_sel:[0,0,1]
	v_readlane_b32 s70, v250, 48
	v_readlane_b32 s71, v250, 49
	s_waitcnt vmcnt(12)
	v_lshlrev_b32_e32 v128, 16, v132
	v_and_b32_e32 v129, 0xffff0000, v132
	v_lshl_add_u64 v[114:115], v[118:119], 1, s[70:71]
	global_store_dwordx4 v[114:115], v[108:111], off
	v_lshlrev_b32_e32 v130, 16, v133
	v_and_b32_e32 v131, 0xffff0000, v133
	v_mul_f32_e32 v110, v121, v121
	v_mul_f32_e32 v111, v123, v123
	v_lshl_add_u64 v[108:109], s[12:13], 0, v[118:119]
	v_fmac_f32_e32 v110, v120, v120
	v_fmac_f32_e32 v111, v122, v122
	global_store_dwordx2 v[108:109], v[112:113], off
	v_add_f32_e32 v110, v110, v111
	v_mul_f32_e32 v111, v125, v125
	v_mul_f32_e32 v112, v127, v127
	v_lshlrev_b32_e32 v132, 16, v134
	v_and_b32_e32 v133, 0xffff0000, v134
	v_fmac_f32_e32 v111, v124, v124
	v_fmac_f32_e32 v112, v126, v126
	v_lshlrev_b32_e32 v134, 16, v135
	v_and_b32_e32 v135, 0xffff0000, v135
	v_add_f32_e32 v111, v111, v112
	v_pk_add_f32 v[106:107], v[106:107], v[130:131]
	v_pk_add_f32 v[104:105], v[104:105], v[128:129]
	v_pk_add_f32 v[100:101], v[100:101], v[132:133]
	v_add_f32_e32 v112, v110, v111
	v_pk_add_f32 v[110:111], v[102:103], v[134:135]
	v_cvt_pk_bf16_f32 v102, v104, v105
	v_cvt_pk_bf16_f32 v103, v106, v107
	v_cvt_pk_bf16_f32 v104, v100, v101
	v_mov_b32_e32 v106, v3
	v_lshlrev_b32_e32 v100, 16, v102
	v_and_b32_e32 v101, 0xffff0000, v102
	v_cvt_pk_bf16_f32 v105, v110, v111
	v_and_b32_e32 v111, 0xffff0000, v103
	v_cvt_pk_fp8_f32 v106, v100, v101
	v_mul_f32_e32 v101, v101, v101
	v_lshlrev_b32_e32 v110, 16, v103
	v_fmac_f32_e32 v101, v100, v100
	v_mul_f32_e32 v100, v111, v111
	v_and_b32_e32 v118, 0xffff0000, v104
	v_fmac_f32_e32 v100, v110, v110
	v_lshlrev_b32_e32 v113, 16, v104
	v_and_b32_e32 v120, 0xffff0000, v105
	v_mov_b32_e32 v107, v3
	v_add_f32_e32 v100, v101, v100
	v_mul_f32_e32 v101, v118, v118
	v_lshlrev_b32_e32 v119, 16, v105
	v_cvt_pk_fp8_f32 v107, v113, v118
	v_fmac_f32_e32 v101, v113, v113
	v_mul_f32_e32 v113, v120, v120
	v_fmac_f32_e32 v113, v119, v119
	v_add_f32_e32 v101, v101, v113
	v_add_f32_e32 v100, v100, v101
	v_add_f32_e32 v100, v112, v100
	ds_bpermute_b32 v101, v116, v100
	v_cvt_pk_fp8_f32 v106, v110, v111 op_sel:[0,0,1]
	v_cvt_pk_fp8_f32 v107, v119, v120 op_sel:[0,0,1]
	v_readlane_b32 s57, v250, 35
	v_readlane_b32 s58, v250, 36
	s_waitcnt lgkmcnt(0)
	v_add_f32_e32 v100, v100, v101
	ds_bpermute_b32 v101, v117, v100
	v_readlane_b32 s59, v250, 37
	v_readlane_b32 s60, v250, 38
	v_readlane_b32 s61, v250, 39
	v_readlane_b32 s62, v250, 40
	v_readlane_b32 s63, v250, 41
	v_readlane_b32 s64, v250, 42
	v_readlane_b32 s65, v250, 43
	v_readlane_b32 s66, v250, 44
	v_readlane_b32 s67, v250, 45
	v_readlane_b32 s68, v250, 46
	v_readlane_b32 s69, v250, 47
	global_store_dwordx4 v[114:115], v[102:105], off offset:256
	global_store_dwordx2 v[108:109], v[106:107], off offset:128
	s_and_saveexec_b64 s[22:23], s[2:3]
	s_cbranch_execz .LBB0_3138
	v_lshlrev_b64 v[102:103], 7, v[148:149]
	v_lshl_add_u64 v[102:103], s[10:11], 0, v[102:103]
	v_lshl_add_u64 v[102:103], s[20:21], 2, v[102:103]
	s_lshl_b32 s0, s42, 2
	v_lshl_add_u64 v[102:103], v[102:103], 0, s[0:1]
	s_waitcnt lgkmcnt(0)
	v_add_f32_e32 v100, v100, v101
	global_store_dword v[102:103], v100, off
; __device__ __forceinline__ float bflo(unsigned x) { return __uint_as_float(x << 16); }
; __device__ __forceinline__ float bfhi(unsigned x) { return __uint_as_float(x & 0xffff0000u); }
; __device__ __forceinline__ unsigned cvtpk(float lo, float hi) { unsigned r; asm volatile("v_cvt_pk_bf16_f32 %0, %1, %2" : "=v"(r) : "v"(lo), "v"(hi)); return r; }
;     __device__ __forceinline__ void operator()(const f32x4 (&acc)[2][2][4][2], const Unit& u, int wr, int wc, int fr, int fq) const {
;     ...
;             for (int mm = 0; mm < 2; ++mm) { const int m = 2 * mh + mm; const size_t off = (size_t)(row0 + ai * HALF + m * 16) * ldc + col0;
; #pragma unroll
;                 for (int bj = 0; bj < 2; ++bj) {
;                     if constexpr (RF32) { const float* p = (const float*)res + off + bj * HALF; r[mm][bj][0] = *(const f32x4*)p; r[mm][bj][1] = *(const f32x4*)(p + 4); }
;                     else { const u32x4 w = *(const u32x4*)((const bf16_t*)res + off + bj * HALF); r[mm][bj][0] = (f32x4){bflo(w.x), bfhi(w.x), bflo(w.y), bfhi(w.y)}; r[mm][bj][1] = (f32x4){bflo(w.z), bfhi(w.z), bflo(w.w), bfhi(w.w)}; } } }
;             asm volatile("" ::: "memory");
; #pragma unroll
;             for (int mm = 0; mm < 2; ++mm) { const int m = 2 * mh + mm; const size_t off = (size_t)(row0 + ai * HALF + m * 16) * ldc + col0; float sq = 0.f;
; #pragma unroll
;                 for (int bj = 0; bj < 2; ++bj) { const f32x4 v0 = r[mm][bj][0] + acc[ai][bj][m][0], v1 = r[mm][bj][1] + acc[ai][bj][m][1];
;                     u32x4 w; w.x = cvtpk(v0[0], v0[1]); w.y = cvtpk(v0[2], v0[3]); w.z = cvtpk(v1[0], v1[1]); w.w = cvtpk(v1[2], v1[3]);
;                     *(u32x4*)(out + off + bj * HALF) = w;
;                     const float a0 = bflo(w.x), a1 = bfhi(w.x), a2 = bflo(w.y), a3 = bfhi(w.y), a4 = bflo(w.z), a5 = bfhi(w.z), a6 = bflo(w.w), a7 = bfhi(w.w);
;                     if (out8) { u32x2 w8; w8.x = pk4_fp8(a0, a1, a2, a3); w8.y = pk4_fp8(a4, a5, a6, a7); *(u32x2*)(out8 + off + bj * HALF) = w8; }
;                     sq += ((a0 * a0 + a1 * a1) + (a2 * a2 + a3 * a3)) + ((a4 * a4 + a5 * a5) + (a6 * a6 + a7 * a7)); }
;                 if (ss) { sq += __shfl_xor(sq, 16); sq += __shfl_xor(sq, 32); if (fq == 0) ss[(size_t)(row0 + ai * HALF + m * 16) * 32 + 4 * u.pn + wc] = sq; } }
.LBB0_3138:
	s_or_b64 exec, exec, s[22:23]
	v_or_b32_e32 v110, 32, v144
	v_ashrrev_i32_e32 v111, 31, v110
	s_waitcnt lgkmcnt(0)
	v_lshlrev_b64 v[100:101], 12, v[110:111]
	v_lshl_add_u64 v[104:105], v[146:147], 0, v[100:101]
	v_or_b32_e32 v108, 48, v144
	v_ashrrev_i32_e32 v109, 31, v108
	v_lshlrev_b64 v[112:113], 11, v[110:111]
	v_readlane_b32 s56, v250, 34
	v_lshl_add_u64 v[112:113], v[112:113], 0, v[142:143]
	v_readlane_b32 s70, v250, 48
	v_readlane_b32 s71, v250, 49
	v_readlane_b32 s57, v250, 35
	v_readlane_b32 s58, v250, 36
	v_readlane_b32 s59, v250, 37
	v_readlane_b32 s60, v250, 38
	v_readlane_b32 s61, v250, 39
	v_readlane_b32 s62, v250, 40
	v_readlane_b32 s63, v250, 41
	v_readlane_b32 s64, v250, 42
	v_readlane_b32 s65, v250, 43
	v_readlane_b32 s66, v250, 44
	v_readlane_b32 s67, v250, 45
	v_readlane_b32 s68, v250, 46
	v_readlane_b32 s69, v250, 47
	s_waitcnt vmcnt(15)
	v_lshlrev_b32_e32 v114, 16, v206
	v_and_b32_e32 v115, 0xffff0000, v206
	v_lshlrev_b32_e32 v118, 16, v207
	v_and_b32_e32 v119, 0xffff0000, v207
	v_lshlrev_b32_e32 v120, 16, v208
	v_and_b32_e32 v121, 0xffff0000, v208
	v_lshlrev_b32_e32 v122, 16, v209
	v_and_b32_e32 v123, 0xffff0000, v209
	v_pk_add_f32 v[96:97], v[96:97], v[114:115]
	v_pk_add_f32 v[114:115], v[94:95], v[122:123]
	v_pk_add_f32 v[94:95], v[92:93], v[120:121]
	v_pk_add_f32 v[98:99], v[98:99], v[118:119]
	s_waitcnt vmcnt(14)
	v_lshlrev_b32_e32 v124, 16, v210
	v_and_b32_e32 v125, 0xffff0000, v210
	v_lshlrev_b32_e32 v126, 16, v211
	v_and_b32_e32 v127, 0xffff0000, v211
	v_lshlrev_b64 v[100:101], 12, v[108:109]
	v_lshl_add_u64 v[100:101], v[146:147], 0, v[100:101]
	v_lshlrev_b32_e32 v128, 16, v212
	v_and_b32_e32 v129, 0xffff0000, v212
	v_lshlrev_b32_e32 v130, 16, v213
	v_and_b32_e32 v131, 0xffff0000, v213
	s_nop 0
	v_cvt_pk_bf16_f32 v92, v96, v97
	v_cvt_pk_bf16_f32 v93, v98, v99
	v_cvt_pk_bf16_f32 v94, v94, v95
	v_cvt_pk_bf16_f32 v95, v114, v115
	v_lshl_add_u64 v[96:97], v[112:113], 1, s[70:71]
	global_store_dwordx4 v[96:97], v[92:95], off
	v_lshlrev_b32_e32 v98, 16, v92
	v_and_b32_e32 v99, 0xffff0000, v92
	v_lshlrev_b32_e32 v118, 16, v94
	v_and_b32_e32 v119, 0xffff0000, v94
	v_lshlrev_b32_e32 v120, 16, v95
	v_and_b32_e32 v121, 0xffff0000, v95
	v_mov_b32_e32 v94, v3
	v_mov_b32_e32 v95, v3
	v_cvt_pk_fp8_f32 v94, v98, v99
	v_cvt_pk_fp8_f32 v95, v118, v119
	v_lshlrev_b32_e32 v114, 16, v93
	v_and_b32_e32 v115, 0xffff0000, v93
	v_cvt_pk_fp8_f32 v94, v114, v115 op_sel:[0,0,1]
	v_cvt_pk_fp8_f32 v95, v120, v121 op_sel:[0,0,1]
	v_lshl_add_u64 v[92:93], s[12:13], 0, v[112:113]
	v_pk_add_f32 v[90:91], v[90:91], v[126:127]
	v_pk_add_f32 v[88:89], v[88:89], v[124:125]
	global_store_dwordx2 v[92:93], v[94:95], off
	v_mul_f32_e32 v94, v99, v99
	v_mul_f32_e32 v95, v115, v115
	v_fmac_f32_e32 v94, v98, v98
	v_fmac_f32_e32 v95, v114, v114
	v_add_f32_e32 v94, v94, v95
	v_mul_f32_e32 v95, v119, v119
	v_mul_f32_e32 v98, v121, v121
	v_fmac_f32_e32 v95, v118, v118
	v_fmac_f32_e32 v98, v120, v120
	v_add_f32_e32 v95, v95, v98
	v_pk_add_f32 v[98:99], v[86:87], v[130:131]
	v_pk_add_f32 v[86:87], v[84:85], v[128:129]
	v_cvt_pk_bf16_f32 v84, v88, v89
	v_cvt_pk_bf16_f32 v85, v90, v91
	v_add_f32_e32 v94, v94, v95
	v_cvt_pk_bf16_f32 v86, v86, v87
	v_cvt_pk_bf16_f32 v87, v98, v99
	global_store_dwordx4 v[96:97], v[84:87], off offset:256
	v_lshlrev_b32_e32 v95, 16, v84
	v_and_b32_e32 v96, 0xffff0000, v84
	v_lshlrev_b32_e32 v90, 16, v85
	v_and_b32_e32 v91, 0xffff0000, v85
	v_lshlrev_b32_e32 v88, 16, v86
	v_and_b32_e32 v89, 0xffff0000, v86
	v_mov_b32_e32 v84, v3
	v_mov_b32_e32 v85, v3
	v_cvt_pk_fp8_f32 v84, v95, v96
	v_cvt_pk_fp8_f32 v85, v88, v89
	v_lshlrev_b32_e32 v86, 16, v87
	v_and_b32_e32 v87, 0xffff0000, v87
	v_cvt_pk_fp8_f32 v84, v90, v91 op_sel:[0,0,1]
	v_cvt_pk_fp8_f32 v85, v86, v87 op_sel:[0,0,1]
	v_mul_f32_e32 v87, v87, v87
	v_fmac_f32_e32 v87, v86, v86
	global_store_dwordx2 v[92:93], v[84:85], off offset:128
	v_mul_f32_e32 v84, v96, v96
	v_mul_f32_e32 v85, v91, v91
	v_fmac_f32_e32 v84, v95, v95
	v_fmac_f32_e32 v85, v90, v90
	v_add_f32_e32 v84, v84, v85
	v_mul_f32_e32 v85, v89, v89
	v_fmac_f32_e32 v85, v88, v88
	v_add_f32_e32 v85, v85, v87
	v_add_f32_e32 v84, v84, v85
	v_add_f32_e32 v84, v94, v84
	ds_bpermute_b32 v85, v116, v84
	s_waitcnt lgkmcnt(0)
	v_add_f32_e32 v84, v84, v85
	ds_bpermute_b32 v85, v117, v84
	s_and_saveexec_b64 s[22:23], s[2:3]
	s_cbranch_execz .LBB0_3140
	v_lshlrev_b64 v[86:87], 7, v[110:111]
	v_lshl_add_u64 v[86:87], s[10:11], 0, v[86:87]
	v_lshl_add_u64 v[86:87], s[20:21], 2, v[86:87]
	s_lshl_b32 s0, s42, 2
	v_lshl_add_u64 v[86:87], v[86:87], 0, s[0:1]
	s_waitcnt lgkmcnt(0)
	v_add_f32_e32 v84, v84, v85
	global_store_dword v[86:87], v84, off
; __device__ __forceinline__ float bflo(unsigned x) { return __uint_as_float(x << 16); }
; __device__ __forceinline__ float bfhi(unsigned x) { return __uint_as_float(x & 0xffff0000u); }
; __device__ __forceinline__ unsigned cvtpk(float lo, float hi) { unsigned r; asm volatile("v_cvt_pk_bf16_f32 %0, %1, %2" : "=v"(r) : "v"(lo), "v"(hi)); return r; }
;     __device__ __forceinline__ void operator()(const f32x4 (&acc)[2][2][4][2], const Unit& u, int wr, int wc, int fr, int fq) const {
;     ...
;             for (int mm = 0; mm < 2; ++mm) { const int m = 2 * mh + mm; const size_t off = (size_t)(row0 + ai * HALF + m * 16) * ldc + col0;
; #pragma unroll
;                 for (int bj = 0; bj < 2; ++bj) {
;                     if constexpr (RF32) { const float* p = (const float*)res + off + bj * HALF; r[mm][bj][0] = *(const f32x4*)p; r[mm][bj][1] = *(const f32x4*)(p + 4); }
;                     else { const u32x4 w = *(const u32x4*)((const bf16_t*)res + off + bj * HALF); r[mm][bj][0] = (f32x4){bflo(w.x), bfhi(w.x), bflo(w.y), bfhi(w.y)}; r[mm][bj][1] = (f32x4){bflo(w.z), bfhi(w.z), bflo(w.w), bfhi(w.w)}; } } }
;             asm volatile("" ::: "memory");
; #pragma unroll
;             for (int mm = 0; mm < 2; ++mm) { const int m = 2 * mh + mm; const size_t off = (size_t)(row0 + ai * HALF + m * 16) * ldc + col0; float sq = 0.f;
; #pragma unroll
;                 for (int bj = 0; bj < 2; ++bj) { const f32x4 v0 = r[mm][bj][0] + acc[ai][bj][m][0], v1 = r[mm][bj][1] + acc[ai][bj][m][1];
;                     u32x4 w; w.x = cvtpk(v0[0], v0[1]); w.y = cvtpk(v0[2], v0[3]); w.z = cvtpk(v1[0], v1[1]); w.w = cvtpk(v1[2], v1[3]);
;                     *(u32x4*)(out + off + bj * HALF) = w;
;                     const float a0 = bflo(w.x), a1 = bfhi(w.x), a2 = bflo(w.y), a3 = bfhi(w.y), a4 = bflo(w.z), a5 = bfhi(w.z), a6 = bflo(w.w), a7 = bfhi(w.w);
;                     if (out8) { u32x2 w8; w8.x = pk4_fp8(a0, a1, a2, a3); w8.y = pk4_fp8(a4, a5, a6, a7); *(u32x2*)(out8 + off + bj * HALF) = w8; }
;                     sq += ((a0 * a0 + a1 * a1) + (a2 * a2 + a3 * a3)) + ((a4 * a4 + a5 * a5) + (a6 * a6 + a7 * a7)); }
;                 if (ss) { sq += __shfl_xor(sq, 16); sq += __shfl_xor(sq, 32); if (fq == 0) ss[(size_t)(row0 + ai * HALF + m * 16) * 32 + 4 * u.pn + wc] = sq; } }
.LBB0_3140:
	s_or_b64 exec, exec, s[22:23]
	s_waitcnt vmcnt(17)
	v_lshlrev_b32_e32 v86, 16, v214
	v_and_b32_e32 v87, 0xffff0000, v214
	v_lshlrev_b32_e32 v90, 16, v216
	v_and_b32_e32 v91, 0xffff0000, v216
	v_lshlrev_b32_e32 v92, 16, v217
	v_and_b32_e32 v93, 0xffff0000, v217
	v_lshlrev_b32_e32 v88, 16, v215
	v_and_b32_e32 v89, 0xffff0000, v215
	v_pk_add_f32 v[80:81], v[80:81], v[86:87]
	v_pk_add_f32 v[86:87], v[78:79], v[92:93]
	v_pk_add_f32 v[78:79], v[76:77], v[90:91]
	v_pk_add_f32 v[82:83], v[82:83], v[88:89]
	v_cvt_pk_bf16_f32 v76, v80, v81
	v_mov_b32_e32 v80, v3
	v_cvt_pk_bf16_f32 v77, v82, v83
	v_cvt_pk_bf16_f32 v78, v78, v79
	v_cvt_pk_bf16_f32 v79, v86, v87
	v_lshlrev_b32_e32 v86, 16, v76
	v_and_b32_e32 v87, 0xffff0000, v76
	v_lshlrev_b32_e32 v90, 16, v78
	v_and_b32_e32 v91, 0xffff0000, v78
	v_mov_b32_e32 v81, v3
	v_cvt_pk_fp8_f32 v80, v86, v87
	v_cvt_pk_fp8_f32 v81, v90, v91
	s_waitcnt lgkmcnt(0)
	v_lshlrev_b64 v[84:85], 11, v[108:109]
	v_lshlrev_b32_e32 v88, 16, v77
	v_and_b32_e32 v89, 0xffff0000, v77
	v_lshlrev_b32_e32 v92, 16, v79
	v_and_b32_e32 v93, 0xffff0000, v79
	v_readlane_b32 s56, v250, 34
	v_lshl_add_u64 v[84:85], v[84:85], 0, v[142:143]
	v_cvt_pk_fp8_f32 v80, v88, v89 op_sel:[0,0,1]
	v_cvt_pk_fp8_f32 v81, v92, v93 op_sel:[0,0,1]
	v_readlane_b32 s70, v250, 48
	v_readlane_b32 s71, v250, 49
	s_waitcnt vmcnt(16)
	v_lshlrev_b32_e32 v94, 16, v218
	v_and_b32_e32 v95, 0xffff0000, v218
	v_lshl_add_u64 v[82:83], v[84:85], 1, s[70:71]
	global_store_dwordx4 v[82:83], v[76:79], off
	v_lshlrev_b32_e32 v96, 16, v219
	v_and_b32_e32 v97, 0xffff0000, v219
	v_mul_f32_e32 v78, v87, v87
	v_mul_f32_e32 v79, v89, v89
	v_lshl_add_u64 v[76:77], s[12:13], 0, v[84:85]
	v_fmac_f32_e32 v78, v86, v86
	v_fmac_f32_e32 v79, v88, v88
	global_store_dwordx2 v[76:77], v[80:81], off
	v_add_f32_e32 v78, v78, v79
	v_mul_f32_e32 v79, v91, v91
	v_mul_f32_e32 v80, v93, v93
	v_lshlrev_b32_e32 v98, 16, v220
	v_and_b32_e32 v99, 0xffff0000, v220
	v_fmac_f32_e32 v79, v90, v90
	v_fmac_f32_e32 v80, v92, v92
	v_lshlrev_b32_e32 v100, 16, v221
	v_and_b32_e32 v101, 0xffff0000, v221
	v_add_f32_e32 v79, v79, v80
	v_pk_add_f32 v[74:75], v[74:75], v[96:97]
	v_pk_add_f32 v[72:73], v[72:73], v[94:95]
	v_pk_add_f32 v[68:69], v[68:69], v[98:99]
	v_add_f32_e32 v80, v78, v79
	v_pk_add_f32 v[78:79], v[70:71], v[100:101]
	v_cvt_pk_bf16_f32 v70, v72, v73
	v_cvt_pk_bf16_f32 v71, v74, v75
	v_cvt_pk_bf16_f32 v72, v68, v69
	v_mov_b32_e32 v74, v3
	v_lshlrev_b32_e32 v68, 16, v70
	v_and_b32_e32 v69, 0xffff0000, v70
	v_cvt_pk_bf16_f32 v73, v78, v79
	v_and_b32_e32 v79, 0xffff0000, v71
	v_cvt_pk_fp8_f32 v74, v68, v69
	v_mul_f32_e32 v69, v69, v69
	v_lshlrev_b32_e32 v78, 16, v71
	v_fmac_f32_e32 v69, v68, v68
	v_mul_f32_e32 v68, v79, v79
	v_and_b32_e32 v84, 0xffff0000, v72
	v_fmac_f32_e32 v68, v78, v78
	v_lshlrev_b32_e32 v81, 16, v72
	v_and_b32_e32 v86, 0xffff0000, v73
	v_mov_b32_e32 v75, v3
	v_add_f32_e32 v68, v69, v68
	v_mul_f32_e32 v69, v84, v84
	v_lshlrev_b32_e32 v85, 16, v73
	v_cvt_pk_fp8_f32 v75, v81, v84
	v_fmac_f32_e32 v69, v81, v81
	v_mul_f32_e32 v81, v86, v86
	v_fmac_f32_e32 v81, v85, v85
	v_add_f32_e32 v69, v69, v81
	v_add_f32_e32 v68, v68, v69
	v_add_f32_e32 v68, v80, v68
	ds_bpermute_b32 v69, v116, v68
	v_cvt_pk_fp8_f32 v74, v78, v79 op_sel:[0,0,1]
	v_cvt_pk_fp8_f32 v75, v85, v86 op_sel:[0,0,1]
	v_readlane_b32 s57, v250, 35
	v_readlane_b32 s58, v250, 36
	s_waitcnt lgkmcnt(0)
	v_add_f32_e32 v68, v68, v69
	ds_bpermute_b32 v69, v117, v68
	v_readlane_b32 s59, v250, 37
	v_readlane_b32 s60, v250, 38
	v_readlane_b32 s61, v250, 39
	v_readlane_b32 s62, v250, 40
	v_readlane_b32 s63, v250, 41
	v_readlane_b32 s64, v250, 42
	v_readlane_b32 s65, v250, 43
	v_readlane_b32 s66, v250, 44
	v_readlane_b32 s67, v250, 45
	v_readlane_b32 s68, v250, 46
	v_readlane_b32 s69, v250, 47
	global_store_dwordx4 v[82:83], v[70:73], off offset:256
	global_store_dwordx2 v[76:77], v[74:75], off offset:128
	s_and_saveexec_b64 s[22:23], s[2:3]
	s_cbranch_execz .LBB0_3142
	v_lshlrev_b64 v[70:71], 7, v[108:109]
	v_lshl_add_u64 v[70:71], s[10:11], 0, v[70:71]
	v_lshl_add_u64 v[70:71], s[20:21], 2, v[70:71]
	s_lshl_b32 s0, s42, 2
	v_lshl_add_u64 v[70:71], v[70:71], 0, s[0:1]
	s_waitcnt lgkmcnt(0)
	v_add_f32_e32 v68, v68, v69
	global_store_dword v[70:71], v68, off
; __device__ __forceinline__ float bflo(unsigned x) { return __uint_as_float(x << 16); }
; __device__ __forceinline__ float bfhi(unsigned x) { return __uint_as_float(x & 0xffff0000u); }
; __device__ __forceinline__ unsigned cvtpk(float lo, float hi) { unsigned r; asm volatile("v_cvt_pk_bf16_f32 %0, %1, %2" : "=v"(r) : "v"(lo), "v"(hi)); return r; }
;     __device__ __forceinline__ void operator()(const f32x4 (&acc)[2][2][4][2], const Unit& u, int wr, int wc, int fr, int fq) const {
;     ...
;             for (int mm = 0; mm < 2; ++mm) { const int m = 2 * mh + mm; const size_t off = (size_t)(row0 + ai * HALF + m * 16) * ldc + col0;
; #pragma unroll
;                 for (int bj = 0; bj < 2; ++bj) {
;                     if constexpr (RF32) { const float* p = (const float*)res + off + bj * HALF; r[mm][bj][0] = *(const f32x4*)p; r[mm][bj][1] = *(const f32x4*)(p + 4); }
;                     else { const u32x4 w = *(const u32x4*)((const bf16_t*)res + off + bj * HALF); r[mm][bj][0] = (f32x4){bflo(w.x), bfhi(w.x), bflo(w.y), bfhi(w.y)}; r[mm][bj][1] = (f32x4){bflo(w.z), bfhi(w.z), bflo(w.w), bfhi(w.w)}; } } }
;             asm volatile("" ::: "memory");
; #pragma unroll
;             for (int mm = 0; mm < 2; ++mm) { const int m = 2 * mh + mm; const size_t off = (size_t)(row0 + ai * HALF + m * 16) * ldc + col0; float sq = 0.f;
; #pragma unroll
;                 for (int bj = 0; bj < 2; ++bj) { const f32x4 v0 = r[mm][bj][0] + acc[ai][bj][m][0], v1 = r[mm][bj][1] + acc[ai][bj][m][1];
;                     u32x4 w; w.x = cvtpk(v0[0], v0[1]); w.y = cvtpk(v0[2], v0[3]); w.z = cvtpk(v1[0], v1[1]); w.w = cvtpk(v1[2], v1[3]);
;                     *(u32x4*)(out + off + bj * HALF) = w;
;                     const float a0 = bflo(w.x), a1 = bfhi(w.x), a2 = bflo(w.y), a3 = bfhi(w.y), a4 = bflo(w.z), a5 = bfhi(w.z), a6 = bflo(w.w), a7 = bfhi(w.w);
;                     if (out8) { u32x2 w8; w8.x = pk4_fp8(a0, a1, a2, a3); w8.y = pk4_fp8(a4, a5, a6, a7); *(u32x2*)(out8 + off + bj * HALF) = w8; }
;                     sq += ((a0 * a0 + a1 * a1) + (a2 * a2 + a3 * a3)) + ((a4 * a4 + a5 * a5) + (a6 * a6 + a7 * a7)); }
;                 if (ss) { sq += __shfl_xor(sq, 16); sq += __shfl_xor(sq, 32); if (fq == 0) ss[(size_t)(row0 + ai * HALF + m * 16) * 32 + 4 * u.pn + wc] = sq; } }
.LBB0_3142:
	s_or_b64 exec, exec, s[22:23]
	v_add_u32_e32 v78, 0x80, v144
	v_ashrrev_i32_e32 v79, 31, v78
	s_waitcnt lgkmcnt(0)
	v_lshlrev_b64 v[68:69], 12, v[78:79]
	v_lshl_add_u64 v[72:73], v[146:147], 0, v[68:69]
	s_mov_b64 s[72:73], 0xa0000
	v_lshl_add_u64 v[182:183], s[72:73], 0, v[180:181]
	global_load_dwordx4 v[206:209], v[182:183], off
	global_load_dwordx4 v[210:213], v[182:183], off offset:256
	s_mov_b64 s[72:73], 0xb0000
	v_lshl_add_u64 v[182:183], s[72:73], 0, v[180:181]
	global_load_dwordx4 v[214:217], v[182:183], off
	global_load_dwordx4 v[218:221], v[182:183], off offset:256
	v_add_u32_e32 v76, 0x90, v144
	v_ashrrev_i32_e32 v77, 31, v76
	v_lshlrev_b64 v[80:81], 11, v[78:79]
	v_readlane_b32 s56, v250, 34
	v_lshl_add_u64 v[80:81], v[80:81], 0, v[142:143]
	v_readlane_b32 s70, v250, 48
	v_readlane_b32 s71, v250, 49
	v_readlane_b32 s57, v250, 35
	v_readlane_b32 s58, v250, 36
	v_readlane_b32 s59, v250, 37
	v_readlane_b32 s60, v250, 38
	v_readlane_b32 s61, v250, 39
	v_readlane_b32 s62, v250, 40
	v_readlane_b32 s63, v250, 41
	v_readlane_b32 s64, v250, 42
	v_readlane_b32 s65, v250, 43
	v_readlane_b32 s66, v250, 44
	v_readlane_b32 s67, v250, 45
	v_readlane_b32 s68, v250, 46
	v_readlane_b32 s69, v250, 47
	s_waitcnt vmcnt(23)
	v_lshlrev_b32_e32 v82, 16, v222
	v_and_b32_e32 v83, 0xffff0000, v222
	v_lshlrev_b32_e32 v84, 16, v223
	v_and_b32_e32 v85, 0xffff0000, v223
	v_lshlrev_b32_e32 v86, 16, v224
	v_and_b32_e32 v87, 0xffff0000, v224
	v_lshlrev_b32_e32 v88, 16, v225
	v_and_b32_e32 v89, 0xffff0000, v225
	v_pk_add_f32 v[64:65], v[64:65], v[82:83]
	v_pk_add_f32 v[82:83], v[62:63], v[88:89]
	v_pk_add_f32 v[62:63], v[60:61], v[86:87]
	v_pk_add_f32 v[66:67], v[66:67], v[84:85]
	s_waitcnt vmcnt(22)
	v_lshlrev_b32_e32 v90, 16, v226
	v_and_b32_e32 v91, 0xffff0000, v226
	v_lshlrev_b32_e32 v92, 16, v227
	v_and_b32_e32 v93, 0xffff0000, v227
	v_lshlrev_b64 v[68:69], 12, v[76:77]
	v_lshl_add_u64 v[68:69], v[146:147], 0, v[68:69]
	v_lshlrev_b32_e32 v94, 16, v228
	v_and_b32_e32 v95, 0xffff0000, v228
	v_lshlrev_b32_e32 v96, 16, v229
	v_and_b32_e32 v97, 0xffff0000, v229
	s_nop 0
	v_cvt_pk_bf16_f32 v60, v64, v65
	v_cvt_pk_bf16_f32 v61, v66, v67
	v_cvt_pk_bf16_f32 v62, v62, v63
	v_cvt_pk_bf16_f32 v63, v82, v83
	v_lshl_add_u64 v[64:65], v[80:81], 1, s[70:71]
	global_store_dwordx4 v[64:65], v[60:63], off
	v_lshlrev_b32_e32 v66, 16, v60
	v_and_b32_e32 v67, 0xffff0000, v60
	v_lshlrev_b32_e32 v84, 16, v62
	v_and_b32_e32 v85, 0xffff0000, v62
	v_lshlrev_b32_e32 v86, 16, v63
	v_and_b32_e32 v87, 0xffff0000, v63
	v_mov_b32_e32 v62, v3
	v_mov_b32_e32 v63, v3
	v_cvt_pk_fp8_f32 v62, v66, v67
	v_cvt_pk_fp8_f32 v63, v84, v85
	v_lshlrev_b32_e32 v82, 16, v61
	v_and_b32_e32 v83, 0xffff0000, v61
	v_cvt_pk_fp8_f32 v62, v82, v83 op_sel:[0,0,1]
	v_cvt_pk_fp8_f32 v63, v86, v87 op_sel:[0,0,1]
	v_lshl_add_u64 v[60:61], s[12:13], 0, v[80:81]
	v_pk_add_f32 v[58:59], v[58:59], v[92:93]
	v_pk_add_f32 v[56:57], v[56:57], v[90:91]
	global_store_dwordx2 v[60:61], v[62:63], off
	v_mul_f32_e32 v62, v67, v67
	v_mul_f32_e32 v63, v83, v83
	v_fmac_f32_e32 v62, v66, v66
	v_fmac_f32_e32 v63, v82, v82
	v_add_f32_e32 v62, v62, v63
	v_mul_f32_e32 v63, v85, v85
	v_mul_f32_e32 v66, v87, v87
	v_fmac_f32_e32 v63, v84, v84
	v_fmac_f32_e32 v66, v86, v86
	v_add_f32_e32 v63, v63, v66
	v_pk_add_f32 v[66:67], v[54:55], v[96:97]
	v_pk_add_f32 v[54:55], v[52:53], v[94:95]
	v_cvt_pk_bf16_f32 v52, v56, v57
	v_cvt_pk_bf16_f32 v53, v58, v59
	v_add_f32_e32 v62, v62, v63
	v_cvt_pk_bf16_f32 v54, v54, v55
	v_cvt_pk_bf16_f32 v55, v66, v67
	global_store_dwordx4 v[64:65], v[52:55], off offset:256
	v_lshlrev_b32_e32 v63, 16, v52
	v_and_b32_e32 v64, 0xffff0000, v52
	v_lshlrev_b32_e32 v58, 16, v53
	v_and_b32_e32 v59, 0xffff0000, v53
	v_lshlrev_b32_e32 v56, 16, v54
	v_and_b32_e32 v57, 0xffff0000, v54
	v_mov_b32_e32 v52, v3
	v_mov_b32_e32 v53, v3
	v_cvt_pk_fp8_f32 v52, v63, v64
	v_cvt_pk_fp8_f32 v53, v56, v57
	v_lshlrev_b32_e32 v54, 16, v55
	v_and_b32_e32 v55, 0xffff0000, v55
	v_cvt_pk_fp8_f32 v52, v58, v59 op_sel:[0,0,1]
	v_cvt_pk_fp8_f32 v53, v54, v55 op_sel:[0,0,1]
	v_mul_f32_e32 v55, v55, v55
	v_fmac_f32_e32 v55, v54, v54
	global_store_dwordx2 v[60:61], v[52:53], off offset:128
	v_mul_f32_e32 v52, v64, v64
	v_mul_f32_e32 v53, v59, v59
	v_fmac_f32_e32 v52, v63, v63
	v_fmac_f32_e32 v53, v58, v58
	v_add_f32_e32 v52, v52, v53
	v_mul_f32_e32 v53, v57, v57
	v_fmac_f32_e32 v53, v56, v56
	v_add_f32_e32 v53, v53, v55
	v_add_f32_e32 v52, v52, v53
	v_add_f32_e32 v52, v62, v52
	ds_bpermute_b32 v53, v116, v52
	s_waitcnt lgkmcnt(0)
	v_add_f32_e32 v52, v52, v53
	ds_bpermute_b32 v53, v117, v52
	s_and_saveexec_b64 s[22:23], s[2:3]
	s_cbranch_execz .LBB0_3144
	v_lshlrev_b64 v[54:55], 7, v[78:79]
	v_lshl_add_u64 v[54:55], s[10:11], 0, v[54:55]
	v_lshl_add_u64 v[54:55], s[20:21], 2, v[54:55]
	s_lshl_b32 s0, s42, 2
	v_lshl_add_u64 v[54:55], v[54:55], 0, s[0:1]
	s_waitcnt lgkmcnt(0)
	v_add_f32_e32 v52, v52, v53
	global_store_dword v[54:55], v52, off
; __device__ __forceinline__ float bflo(unsigned x) { return __uint_as_float(x << 16); }
; __device__ __forceinline__ float bfhi(unsigned x) { return __uint_as_float(x & 0xffff0000u); }
; __device__ __forceinline__ unsigned cvtpk(float lo, float hi) { unsigned r; asm volatile("v_cvt_pk_bf16_f32 %0, %1, %2" : "=v"(r) : "v"(lo), "v"(hi)); return r; }
;     __device__ __forceinline__ void operator()(const f32x4 (&acc)[2][2][4][2], const Unit& u, int wr, int wc, int fr, int fq) const {
;     ...
;             for (int mm = 0; mm < 2; ++mm) { const int m = 2 * mh + mm; const size_t off = (size_t)(row0 + ai * HALF + m * 16) * ldc + col0;
; #pragma unroll
;                 for (int bj = 0; bj < 2; ++bj) {
;                     if constexpr (RF32) { const float* p = (const float*)res + off + bj * HALF; r[mm][bj][0] = *(const f32x4*)p; r[mm][bj][1] = *(const f32x4*)(p + 4); }
;                     else { const u32x4 w = *(const u32x4*)((const bf16_t*)res + off + bj * HALF); r[mm][bj][0] = (f32x4){bflo(w.x), bfhi(w.x), bflo(w.y), bfhi(w.y)}; r[mm][bj][1] = (f32x4){bflo(w.z), bfhi(w.z), bflo(w.w), bfhi(w.w)}; } } }
;             asm volatile("" ::: "memory");
; #pragma unroll
;             for (int mm = 0; mm < 2; ++mm) { const int m = 2 * mh + mm; const size_t off = (size_t)(row0 + ai * HALF + m * 16) * ldc + col0; float sq = 0.f;
; #pragma unroll
;                 for (int bj = 0; bj < 2; ++bj) { const f32x4 v0 = r[mm][bj][0] + acc[ai][bj][m][0], v1 = r[mm][bj][1] + acc[ai][bj][m][1];
;                     u32x4 w; w.x = cvtpk(v0[0], v0[1]); w.y = cvtpk(v0[2], v0[3]); w.z = cvtpk(v1[0], v1[1]); w.w = cvtpk(v1[2], v1[3]);
;                     *(u32x4*)(out + off + bj * HALF) = w;
;                     const float a0 = bflo(w.x), a1 = bfhi(w.x), a2 = bflo(w.y), a3 = bfhi(w.y), a4 = bflo(w.z), a5 = bfhi(w.z), a6 = bflo(w.w), a7 = bfhi(w.w);
;                     if (out8) { u32x2 w8; w8.x = pk4_fp8(a0, a1, a2, a3); w8.y = pk4_fp8(a4, a5, a6, a7); *(u32x2*)(out8 + off + bj * HALF) = w8; }
;                     sq += ((a0 * a0 + a1 * a1) + (a2 * a2 + a3 * a3)) + ((a4 * a4 + a5 * a5) + (a6 * a6 + a7 * a7)); }
;                 if (ss) { sq += __shfl_xor(sq, 16); sq += __shfl_xor(sq, 32); if (fq == 0) ss[(size_t)(row0 + ai * HALF + m * 16) * 32 + 4 * u.pn + wc] = sq; } }
.LBB0_3144:
	s_or_b64 exec, exec, s[22:23]
	s_waitcnt vmcnt(25)
	v_lshlrev_b32_e32 v54, 16, v230
	v_and_b32_e32 v55, 0xffff0000, v230
	v_lshlrev_b32_e32 v58, 16, v232
	v_and_b32_e32 v59, 0xffff0000, v232
	v_lshlrev_b32_e32 v60, 16, v233
	v_and_b32_e32 v61, 0xffff0000, v233
	v_lshlrev_b32_e32 v56, 16, v231
	v_and_b32_e32 v57, 0xffff0000, v231
	v_pk_add_f32 v[48:49], v[48:49], v[54:55]
	v_pk_add_f32 v[54:55], v[46:47], v[60:61]
	v_pk_add_f32 v[46:47], v[44:45], v[58:59]
	v_pk_add_f32 v[50:51], v[50:51], v[56:57]
	v_cvt_pk_bf16_f32 v44, v48, v49
	v_mov_b32_e32 v48, v3
	v_cvt_pk_bf16_f32 v45, v50, v51
	v_cvt_pk_bf16_f32 v46, v46, v47
	v_cvt_pk_bf16_f32 v47, v54, v55
	v_lshlrev_b32_e32 v54, 16, v44
	v_and_b32_e32 v55, 0xffff0000, v44
	v_lshlrev_b32_e32 v58, 16, v46
	v_and_b32_e32 v59, 0xffff0000, v46
	v_mov_b32_e32 v49, v3
	v_cvt_pk_fp8_f32 v48, v54, v55
	v_cvt_pk_fp8_f32 v49, v58, v59
	s_waitcnt lgkmcnt(0)
	v_lshlrev_b64 v[52:53], 11, v[76:77]
	v_lshlrev_b32_e32 v56, 16, v45
	v_and_b32_e32 v57, 0xffff0000, v45
	v_lshlrev_b32_e32 v60, 16, v47
	v_and_b32_e32 v61, 0xffff0000, v47
	v_readlane_b32 s56, v250, 34
	v_lshl_add_u64 v[52:53], v[52:53], 0, v[142:143]
	v_cvt_pk_fp8_f32 v48, v56, v57 op_sel:[0,0,1]
	v_cvt_pk_fp8_f32 v49, v60, v61 op_sel:[0,0,1]
	v_readlane_b32 s70, v250, 48
	v_readlane_b32 s71, v250, 49
	s_waitcnt vmcnt(24)
	v_lshlrev_b32_e32 v62, 16, v234
	v_and_b32_e32 v63, 0xffff0000, v234
	v_lshl_add_u64 v[50:51], v[52:53], 1, s[70:71]
	global_store_dwordx4 v[50:51], v[44:47], off
	v_lshlrev_b32_e32 v64, 16, v235
	v_and_b32_e32 v65, 0xffff0000, v235
	v_mul_f32_e32 v46, v55, v55
	v_mul_f32_e32 v47, v57, v57
	v_lshl_add_u64 v[44:45], s[12:13], 0, v[52:53]
	v_fmac_f32_e32 v46, v54, v54
	v_fmac_f32_e32 v47, v56, v56
	global_store_dwordx2 v[44:45], v[48:49], off
	v_add_f32_e32 v46, v46, v47
	v_mul_f32_e32 v47, v59, v59
	v_mul_f32_e32 v48, v61, v61
	v_lshlrev_b32_e32 v66, 16, v236
	v_and_b32_e32 v67, 0xffff0000, v236
	v_fmac_f32_e32 v47, v58, v58
	v_fmac_f32_e32 v48, v60, v60
	v_lshlrev_b32_e32 v68, 16, v237
	v_and_b32_e32 v69, 0xffff0000, v237
	v_add_f32_e32 v47, v47, v48
	v_pk_add_f32 v[42:43], v[42:43], v[64:65]
	v_pk_add_f32 v[40:41], v[40:41], v[62:63]
	v_pk_add_f32 v[36:37], v[36:37], v[66:67]
	v_add_f32_e32 v48, v46, v47
	v_pk_add_f32 v[46:47], v[38:39], v[68:69]
	v_cvt_pk_bf16_f32 v38, v40, v41
	v_cvt_pk_bf16_f32 v39, v42, v43
	v_cvt_pk_bf16_f32 v40, v36, v37
	v_mov_b32_e32 v42, v3
	v_lshlrev_b32_e32 v36, 16, v38
	v_and_b32_e32 v37, 0xffff0000, v38
	v_cvt_pk_bf16_f32 v41, v46, v47
	v_and_b32_e32 v47, 0xffff0000, v39
	v_cvt_pk_fp8_f32 v42, v36, v37
	v_mul_f32_e32 v37, v37, v37
	v_lshlrev_b32_e32 v46, 16, v39
	v_fmac_f32_e32 v37, v36, v36
	v_mul_f32_e32 v36, v47, v47
	v_and_b32_e32 v52, 0xffff0000, v40
	v_fmac_f32_e32 v36, v46, v46
	v_lshlrev_b32_e32 v49, 16, v40
	v_and_b32_e32 v54, 0xffff0000, v41
	v_mov_b32_e32 v43, v3
	v_add_f32_e32 v36, v37, v36
	v_mul_f32_e32 v37, v52, v52
	v_lshlrev_b32_e32 v53, 16, v41
	v_cvt_pk_fp8_f32 v43, v49, v52
	v_fmac_f32_e32 v37, v49, v49
	v_mul_f32_e32 v49, v54, v54
	v_fmac_f32_e32 v49, v53, v53
	v_add_f32_e32 v37, v37, v49
	v_add_f32_e32 v36, v36, v37
	v_add_f32_e32 v36, v48, v36
	ds_bpermute_b32 v37, v116, v36
	v_cvt_pk_fp8_f32 v42, v46, v47 op_sel:[0,0,1]
	v_cvt_pk_fp8_f32 v43, v53, v54 op_sel:[0,0,1]
	v_readlane_b32 s57, v250, 35
	v_readlane_b32 s58, v250, 36
	s_waitcnt lgkmcnt(0)
	v_add_f32_e32 v36, v36, v37
	ds_bpermute_b32 v37, v117, v36
	v_readlane_b32 s59, v250, 37
	v_readlane_b32 s60, v250, 38
	v_readlane_b32 s61, v250, 39
	v_readlane_b32 s62, v250, 40
	v_readlane_b32 s63, v250, 41
	v_readlane_b32 s64, v250, 42
	v_readlane_b32 s65, v250, 43
	v_readlane_b32 s66, v250, 44
	v_readlane_b32 s67, v250, 45
	v_readlane_b32 s68, v250, 46
	v_readlane_b32 s69, v250, 47
	global_store_dwordx4 v[50:51], v[38:41], off offset:256
	global_store_dwordx2 v[44:45], v[42:43], off offset:128
	s_and_saveexec_b64 s[22:23], s[2:3]
	s_cbranch_execz .LBB0_3146
	v_lshlrev_b64 v[38:39], 7, v[76:77]
	v_lshl_add_u64 v[38:39], s[10:11], 0, v[38:39]
	v_lshl_add_u64 v[38:39], s[20:21], 2, v[38:39]
	s_lshl_b32 s0, s42, 2
	v_lshl_add_u64 v[38:39], v[38:39], 0, s[0:1]
	s_waitcnt lgkmcnt(0)
	v_add_f32_e32 v36, v36, v37
	global_store_dword v[38:39], v36, off
; __device__ __forceinline__ float bflo(unsigned x) { return __uint_as_float(x << 16); }
; __device__ __forceinline__ float bfhi(unsigned x) { return __uint_as_float(x & 0xffff0000u); }
; __device__ __forceinline__ unsigned cvtpk(float lo, float hi) { unsigned r; asm volatile("v_cvt_pk_bf16_f32 %0, %1, %2" : "=v"(r) : "v"(lo), "v"(hi)); return r; }
;     __device__ __forceinline__ void operator()(const f32x4 (&acc)[2][2][4][2], const Unit& u, int wr, int wc, int fr, int fq) const {
;     ...
;             for (int mm = 0; mm < 2; ++mm) { const int m = 2 * mh + mm; const size_t off = (size_t)(row0 + ai * HALF + m * 16) * ldc + col0;
; #pragma unroll
;                 for (int bj = 0; bj < 2; ++bj) {
;                     if constexpr (RF32) { const float* p = (const float*)res + off + bj * HALF; r[mm][bj][0] = *(const f32x4*)p; r[mm][bj][1] = *(const f32x4*)(p + 4); }
;                     else { const u32x4 w = *(const u32x4*)((const bf16_t*)res + off + bj * HALF); r[mm][bj][0] = (f32x4){bflo(w.x), bfhi(w.x), bflo(w.y), bfhi(w.y)}; r[mm][bj][1] = (f32x4){bflo(w.z), bfhi(w.z), bflo(w.w), bfhi(w.w)}; } } }
;             asm volatile("" ::: "memory");
; #pragma unroll
;             for (int mm = 0; mm < 2; ++mm) { const int m = 2 * mh + mm; const size_t off = (size_t)(row0 + ai * HALF + m * 16) * ldc + col0; float sq = 0.f;
; #pragma unroll
;                 for (int bj = 0; bj < 2; ++bj) { const f32x4 v0 = r[mm][bj][0] + acc[ai][bj][m][0], v1 = r[mm][bj][1] + acc[ai][bj][m][1];
;                     u32x4 w; w.x = cvtpk(v0[0], v0[1]); w.y = cvtpk(v0[2], v0[3]); w.z = cvtpk(v1[0], v1[1]); w.w = cvtpk(v1[2], v1[3]);
;                     *(u32x4*)(out + off + bj * HALF) = w;
;                     const float a0 = bflo(w.x), a1 = bfhi(w.x), a2 = bflo(w.y), a3 = bfhi(w.y), a4 = bflo(w.z), a5 = bfhi(w.z), a6 = bflo(w.w), a7 = bfhi(w.w);
;                     if (out8) { u32x2 w8; w8.x = pk4_fp8(a0, a1, a2, a3); w8.y = pk4_fp8(a4, a5, a6, a7); *(u32x2*)(out8 + off + bj * HALF) = w8; }
;                     sq += ((a0 * a0 + a1 * a1) + (a2 * a2 + a3 * a3)) + ((a4 * a4 + a5 * a5) + (a6 * a6 + a7 * a7)); }
;                 if (ss) { sq += __shfl_xor(sq, 16); sq += __shfl_xor(sq, 32); if (fq == 0) ss[(size_t)(row0 + ai * HALF + m * 16) * 32 + 4 * u.pn + wc] = sq; } }
.LBB0_3146:
	s_or_b64 exec, exec, s[22:23]
	v_add_u32_e32 v46, 0xa0, v144
	v_ashrrev_i32_e32 v47, 31, v46
	s_waitcnt lgkmcnt(0)
	v_lshlrev_b64 v[36:37], 12, v[46:47]
	v_lshl_add_u64 v[40:41], v[146:147], 0, v[36:37]
	v_add_u32_e32 v44, 0xb0, v144
	v_ashrrev_i32_e32 v45, 31, v44
	v_lshlrev_b64 v[48:49], 11, v[46:47]
	v_readlane_b32 s56, v250, 34
	v_lshl_add_u64 v[48:49], v[48:49], 0, v[142:143]
	v_readlane_b32 s70, v250, 48
	v_readlane_b32 s71, v250, 49
	v_readlane_b32 s57, v250, 35
	v_readlane_b32 s58, v250, 36
	v_readlane_b32 s59, v250, 37
	v_readlane_b32 s60, v250, 38
	v_readlane_b32 s61, v250, 39
	v_readlane_b32 s62, v250, 40
	v_readlane_b32 s63, v250, 41
	v_readlane_b32 s64, v250, 42
	v_readlane_b32 s65, v250, 43
	v_readlane_b32 s66, v250, 44
	v_readlane_b32 s67, v250, 45
	v_readlane_b32 s68, v250, 46
	v_readlane_b32 s69, v250, 47
	s_waitcnt vmcnt(11)
	v_lshlrev_b32_e32 v50, 16, v206
	v_and_b32_e32 v51, 0xffff0000, v206
	v_lshlrev_b32_e32 v52, 16, v207
	v_and_b32_e32 v53, 0xffff0000, v207
	v_lshlrev_b32_e32 v54, 16, v208
	v_and_b32_e32 v55, 0xffff0000, v208
	v_lshlrev_b32_e32 v56, 16, v209
	v_and_b32_e32 v57, 0xffff0000, v209
	v_pk_add_f32 v[32:33], v[32:33], v[50:51]
	v_pk_add_f32 v[50:51], v[30:31], v[56:57]
	v_pk_add_f32 v[30:31], v[28:29], v[54:55]
	v_pk_add_f32 v[34:35], v[34:35], v[52:53]
	s_waitcnt vmcnt(10)
	v_lshlrev_b32_e32 v58, 16, v210
	v_and_b32_e32 v59, 0xffff0000, v210
	v_lshlrev_b32_e32 v60, 16, v211
	v_and_b32_e32 v61, 0xffff0000, v211
	v_lshlrev_b64 v[36:37], 12, v[44:45]
	v_lshl_add_u64 v[36:37], v[146:147], 0, v[36:37]
	v_lshlrev_b32_e32 v62, 16, v212
	v_and_b32_e32 v63, 0xffff0000, v212
	v_lshlrev_b32_e32 v64, 16, v213
	v_and_b32_e32 v65, 0xffff0000, v213
	s_nop 0
	v_cvt_pk_bf16_f32 v28, v32, v33
	v_cvt_pk_bf16_f32 v29, v34, v35
	v_cvt_pk_bf16_f32 v30, v30, v31
	v_cvt_pk_bf16_f32 v31, v50, v51
	v_lshl_add_u64 v[32:33], v[48:49], 1, s[70:71]
	global_store_dwordx4 v[32:33], v[28:31], off
	v_lshlrev_b32_e32 v34, 16, v28
	v_and_b32_e32 v35, 0xffff0000, v28
	v_lshlrev_b32_e32 v52, 16, v30
	v_and_b32_e32 v53, 0xffff0000, v30
	v_lshlrev_b32_e32 v54, 16, v31
	v_and_b32_e32 v55, 0xffff0000, v31
	v_mov_b32_e32 v30, v3
	v_mov_b32_e32 v31, v3
	v_cvt_pk_fp8_f32 v30, v34, v35
	v_cvt_pk_fp8_f32 v31, v52, v53
	v_lshlrev_b32_e32 v50, 16, v29
	v_and_b32_e32 v51, 0xffff0000, v29
	v_cvt_pk_fp8_f32 v30, v50, v51 op_sel:[0,0,1]
	v_cvt_pk_fp8_f32 v31, v54, v55 op_sel:[0,0,1]
	v_lshl_add_u64 v[28:29], s[12:13], 0, v[48:49]
	v_pk_add_f32 v[26:27], v[26:27], v[60:61]
	v_pk_add_f32 v[24:25], v[24:25], v[58:59]
	global_store_dwordx2 v[28:29], v[30:31], off
	v_mul_f32_e32 v30, v35, v35
	v_mul_f32_e32 v31, v51, v51
	v_fmac_f32_e32 v30, v34, v34
	v_fmac_f32_e32 v31, v50, v50
	v_add_f32_e32 v30, v30, v31
	v_mul_f32_e32 v31, v53, v53
	v_mul_f32_e32 v34, v55, v55
	v_fmac_f32_e32 v31, v52, v52
	v_fmac_f32_e32 v34, v54, v54
	v_add_f32_e32 v31, v31, v34
	v_pk_add_f32 v[34:35], v[22:23], v[64:65]
	v_pk_add_f32 v[22:23], v[20:21], v[62:63]
	v_cvt_pk_bf16_f32 v20, v24, v25
	v_cvt_pk_bf16_f32 v21, v26, v27
	v_add_f32_e32 v30, v30, v31
	v_cvt_pk_bf16_f32 v22, v22, v23
	v_cvt_pk_bf16_f32 v23, v34, v35
	global_store_dwordx4 v[32:33], v[20:23], off offset:256
	v_lshlrev_b32_e32 v31, 16, v20
	v_and_b32_e32 v32, 0xffff0000, v20
	v_lshlrev_b32_e32 v26, 16, v21
	v_and_b32_e32 v27, 0xffff0000, v21
	v_lshlrev_b32_e32 v24, 16, v22
	v_and_b32_e32 v25, 0xffff0000, v22
	v_mov_b32_e32 v20, v3
	v_mov_b32_e32 v21, v3
	v_cvt_pk_fp8_f32 v20, v31, v32
	v_cvt_pk_fp8_f32 v21, v24, v25
	v_lshlrev_b32_e32 v22, 16, v23
	v_and_b32_e32 v23, 0xffff0000, v23
	v_cvt_pk_fp8_f32 v20, v26, v27 op_sel:[0,0,1]
	v_cvt_pk_fp8_f32 v21, v22, v23 op_sel:[0,0,1]
	v_mul_f32_e32 v23, v23, v23
	v_fmac_f32_e32 v23, v22, v22
	global_store_dwordx2 v[28:29], v[20:21], off offset:128
	v_mul_f32_e32 v20, v32, v32
	v_mul_f32_e32 v21, v27, v27
	v_fmac_f32_e32 v20, v31, v31
	v_fmac_f32_e32 v21, v26, v26
	v_add_f32_e32 v20, v20, v21
	v_mul_f32_e32 v21, v25, v25
	v_fmac_f32_e32 v21, v24, v24
	v_add_f32_e32 v21, v21, v23
	v_add_f32_e32 v20, v20, v21
	v_add_f32_e32 v20, v30, v20
	ds_bpermute_b32 v21, v116, v20
	s_waitcnt lgkmcnt(0)
	v_add_f32_e32 v20, v20, v21
	ds_bpermute_b32 v21, v117, v20
	s_and_saveexec_b64 s[22:23], s[2:3]
	s_cbranch_execz .LBB0_3148
	v_lshlrev_b64 v[22:23], 7, v[46:47]
	v_lshl_add_u64 v[22:23], s[10:11], 0, v[22:23]
	v_lshl_add_u64 v[22:23], s[20:21], 2, v[22:23]
	s_lshl_b32 s0, s42, 2
	v_lshl_add_u64 v[22:23], v[22:23], 0, s[0:1]
	s_waitcnt lgkmcnt(0)
	v_add_f32_e32 v20, v20, v21
	global_store_dword v[22:23], v20, off
; __device__ __forceinline__ float bflo(unsigned x) { return __uint_as_float(x << 16); }
; __device__ __forceinline__ float bfhi(unsigned x) { return __uint_as_float(x & 0xffff0000u); }
; __device__ __forceinline__ unsigned cvtpk(float lo, float hi) { unsigned r; asm volatile("v_cvt_pk_bf16_f32 %0, %1, %2" : "=v"(r) : "v"(lo), "v"(hi)); return r; }
; __device__ __forceinline__ unsigned pk4_fp8(float a, float b, float c, float d) { int p = __builtin_amdgcn_cvt_pk_fp8_f32(a, b, 0, false); p = __builtin_amdgcn_cvt_pk_fp8_f32(c, d, p, true); return (unsigned)p; }
;     __device__ __forceinline__ void operator()(const f32x4 (&acc)[2][2][4][2], const Unit& u, int wr, int wc, int fr, int fq) const {
;     ...
;             for (int mm = 0; mm < 2; ++mm) { const int m = 2 * mh + mm; const size_t off = (size_t)(row0 + ai * HALF + m * 16) * ldc + col0; float sq = 0.f;
; #pragma unroll
;                 for (int bj = 0; bj < 2; ++bj) { const f32x4 v0 = r[mm][bj][0] + acc[ai][bj][m][0], v1 = r[mm][bj][1] + acc[ai][bj][m][1];
;                     u32x4 w; w.x = cvtpk(v0[0], v0[1]); w.y = cvtpk(v0[2], v0[3]); w.z = cvtpk(v1[0], v1[1]); w.w = cvtpk(v1[2], v1[3]);
;                     *(u32x4*)(out + off + bj * HALF) = w;
;                     const float a0 = bflo(w.x), a1 = bfhi(w.x), a2 = bflo(w.y), a3 = bfhi(w.y), a4 = bflo(w.z), a5 = bfhi(w.z), a6 = bflo(w.w), a7 = bfhi(w.w);
;                     if (out8) { u32x2 w8; w8.x = pk4_fp8(a0, a1, a2, a3); w8.y = pk4_fp8(a4, a5, a6, a7); *(u32x2*)(out8 + off + bj * HALF) = w8; }
;                     sq += ((a0 * a0 + a1 * a1) + (a2 * a2 + a3 * a3)) + ((a4 * a4 + a5 * a5) + (a6 * a6 + a7 * a7)); }
;                 if (ss) { sq += __shfl_xor(sq, 16); sq += __shfl_xor(sq, 32); if (fq == 0) ss[(size_t)(row0 + ai * HALF + m * 16) * 32 + 4 * u.pn + wc] = sq; } }
.LBB0_3148:
	s_or_b64 exec, exec, s[22:23]
	s_waitcnt vmcnt(13)
	v_lshlrev_b32_e32 v22, 16, v214
	v_and_b32_e32 v23, 0xffff0000, v214
	v_lshlrev_b32_e32 v26, 16, v216
	v_and_b32_e32 v27, 0xffff0000, v216
	v_lshlrev_b32_e32 v28, 16, v217
	v_and_b32_e32 v29, 0xffff0000, v217
	v_lshlrev_b32_e32 v24, 16, v215
	v_and_b32_e32 v25, 0xffff0000, v215
	v_pk_add_f32 v[16:17], v[16:17], v[22:23]
	v_pk_add_f32 v[22:23], v[14:15], v[28:29]
	v_pk_add_f32 v[14:15], v[12:13], v[26:27]
	v_pk_add_f32 v[18:19], v[18:19], v[24:25]
	v_cvt_pk_bf16_f32 v12, v16, v17
	v_mov_b32_e32 v16, v3
	v_cvt_pk_bf16_f32 v13, v18, v19
	v_cvt_pk_bf16_f32 v14, v14, v15
	v_cvt_pk_bf16_f32 v15, v22, v23
	v_lshlrev_b32_e32 v22, 16, v12
	v_and_b32_e32 v23, 0xffff0000, v12
	v_lshlrev_b32_e32 v26, 16, v14
	v_and_b32_e32 v27, 0xffff0000, v14
	v_mov_b32_e32 v17, v3
	v_cvt_pk_fp8_f32 v16, v22, v23
	v_cvt_pk_fp8_f32 v17, v26, v27
	s_waitcnt lgkmcnt(0)
	v_lshlrev_b64 v[20:21], 11, v[44:45]
	v_lshlrev_b32_e32 v24, 16, v13
	v_and_b32_e32 v25, 0xffff0000, v13
	v_lshlrev_b32_e32 v28, 16, v15
	v_and_b32_e32 v29, 0xffff0000, v15
	v_readlane_b32 s56, v250, 34
	v_lshl_add_u64 v[20:21], v[20:21], 0, v[142:143]
	v_cvt_pk_fp8_f32 v16, v24, v25 op_sel:[0,0,1]
	v_cvt_pk_fp8_f32 v17, v28, v29 op_sel:[0,0,1]
	v_readlane_b32 s70, v250, 48
	v_readlane_b32 s71, v250, 49
	s_waitcnt vmcnt(12)
	v_lshlrev_b32_e32 v30, 16, v218
	v_and_b32_e32 v31, 0xffff0000, v218
	v_lshl_add_u64 v[18:19], v[20:21], 1, s[70:71]
	global_store_dwordx4 v[18:19], v[12:15], off
	v_lshlrev_b32_e32 v32, 16, v219
	v_and_b32_e32 v33, 0xffff0000, v219
	v_mul_f32_e32 v14, v23, v23
	v_mul_f32_e32 v15, v25, v25
	v_lshl_add_u64 v[12:13], s[12:13], 0, v[20:21]
	v_fmac_f32_e32 v14, v22, v22
	v_fmac_f32_e32 v15, v24, v24
	global_store_dwordx2 v[12:13], v[16:17], off
	v_add_f32_e32 v14, v14, v15
	v_mul_f32_e32 v15, v27, v27
	v_mul_f32_e32 v16, v29, v29
	v_lshlrev_b32_e32 v34, 16, v220
	v_and_b32_e32 v35, 0xffff0000, v220
	v_fmac_f32_e32 v15, v26, v26
	v_fmac_f32_e32 v16, v28, v28
	v_lshlrev_b32_e32 v36, 16, v221
	v_and_b32_e32 v37, 0xffff0000, v221
	v_add_f32_e32 v15, v15, v16
	v_pk_add_f32 v[10:11], v[10:11], v[32:33]
	v_pk_add_f32 v[8:9], v[8:9], v[30:31]
	v_pk_add_f32 v[4:5], v[4:5], v[34:35]
	v_add_f32_e32 v16, v14, v15
	v_pk_add_f32 v[14:15], v[6:7], v[36:37]
	v_cvt_pk_bf16_f32 v6, v8, v9
	v_cvt_pk_bf16_f32 v7, v10, v11
	v_cvt_pk_bf16_f32 v8, v4, v5
	v_mov_b32_e32 v10, v3
	v_lshlrev_b32_e32 v4, 16, v6
	v_and_b32_e32 v5, 0xffff0000, v6
	v_cvt_pk_bf16_f32 v9, v14, v15
	v_and_b32_e32 v15, 0xffff0000, v7
	v_cvt_pk_fp8_f32 v10, v4, v5
	v_mul_f32_e32 v5, v5, v5
	v_lshlrev_b32_e32 v14, 16, v7
	v_fmac_f32_e32 v5, v4, v4
	v_mul_f32_e32 v4, v15, v15
	v_and_b32_e32 v20, 0xffff0000, v8
	v_fmac_f32_e32 v4, v14, v14
	v_lshlrev_b32_e32 v17, 16, v8
	v_and_b32_e32 v22, 0xffff0000, v9
	v_mov_b32_e32 v11, v3
	v_add_f32_e32 v4, v5, v4
	v_mul_f32_e32 v5, v20, v20
	v_lshlrev_b32_e32 v21, 16, v9
	v_cvt_pk_fp8_f32 v11, v17, v20
	v_fmac_f32_e32 v5, v17, v17
	v_mul_f32_e32 v17, v22, v22
	v_fmac_f32_e32 v17, v21, v21
	v_add_f32_e32 v5, v5, v17
	v_add_f32_e32 v4, v4, v5
	v_add_f32_e32 v4, v16, v4
	ds_bpermute_b32 v5, v116, v4
	v_cvt_pk_fp8_f32 v10, v14, v15 op_sel:[0,0,1]
	v_cvt_pk_fp8_f32 v11, v21, v22 op_sel:[0,0,1]
	v_readlane_b32 s57, v250, 35
	v_readlane_b32 s58, v250, 36
	s_waitcnt lgkmcnt(0)
	v_add_f32_e32 v4, v4, v5
	ds_bpermute_b32 v5, v117, v4
	v_readlane_b32 s59, v250, 37
	v_readlane_b32 s60, v250, 38
	v_readlane_b32 s61, v250, 39
	v_readlane_b32 s62, v250, 40
	v_readlane_b32 s63, v250, 41
	v_readlane_b32 s64, v250, 42
	v_readlane_b32 s65, v250, 43
	v_readlane_b32 s66, v250, 44
	v_readlane_b32 s67, v250, 45
	v_readlane_b32 s68, v250, 46
	v_readlane_b32 s69, v250, 47
	global_store_dwordx4 v[18:19], v[6:9], off offset:256
	global_store_dwordx2 v[12:13], v[10:11], off offset:128
	s_and_saveexec_b64 s[22:23], s[2:3]
	s_cbranch_execz .LBB0_3150
	v_lshlrev_b64 v[6:7], 7, v[44:45]
	v_lshl_add_u64 v[6:7], s[10:11], 0, v[6:7]
	v_lshl_add_u64 v[6:7], s[20:21], 2, v[6:7]
	s_lshl_b32 s0, s42, 2
	v_lshl_add_u64 v[6:7], v[6:7], 0, s[0:1]
	s_waitcnt lgkmcnt(0)
	v_add_f32_e32 v4, v4, v5
	global_store_dword v[6:7], v4, off
